# speedup vs baseline: 1.0104x; 1.0104x over previous
.LBB3_11:
	s_and_b64 vcc, exec, s[4:5]
	s_cbranch_vccz .LBB3_14
	s_add_i32 s19, s2, 0xfffffe00
	s_load_dwordx2 s[20:21], s[0:1], 0x88
	s_load_dwordx2 s[22:23], s[0:1], 0xc0
	s_load_dwordx2 s[24:25], s[0:1], 0xf8
	s_load_dwordx2 s[26:27], s[0:1], 0x130
	s_load_dwordx2 s[28:29], s[0:1], 0x168
	s_load_dwordx4 s[32:35], s[0:1], 0x1a0
	s_mov_b32 s3, 0
	s_waitcnt lgkmcnt(0)
	s_cmp_ge_i32 s19, s20
	s_cselect_b32 s36, 1, 0
	s_cmp_gt_i32 s34, 1
	s_cselect_b32 s37, 1, 0
	s_and_b32 s36, s36, s37
	s_cselect_b32 s3, 1, s3
	s_cmp_ge_i32 s19, s22
	s_cselect_b32 s36, 1, 0
	s_cmp_gt_i32 s34, 2
	s_cselect_b32 s37, 1, 0
	s_and_b32 s36, s36, s37
	s_cselect_b32 s3, 2, s3
	s_cmp_ge_i32 s19, s24
	s_cselect_b32 s36, 1, 0
	s_cmp_gt_i32 s34, 3
	s_cselect_b32 s37, 1, 0
	s_and_b32 s36, s36, s37
	s_cselect_b32 s3, 3, s3
	s_cmp_ge_i32 s19, s26
	s_cselect_b32 s36, 1, 0
	s_cmp_gt_i32 s34, 4
	s_cselect_b32 s37, 1, 0
	s_and_b32 s36, s36, s37
	s_cselect_b32 s3, 4, s3
	s_cmp_ge_i32 s19, s28
	s_cselect_b32 s36, 1, 0
	s_cmp_gt_i32 s34, 5
	s_cselect_b32 s37, 1, 0
	s_and_b32 s36, s36, s37
	s_cselect_b32 s3, 5, s3
	s_cmp_ge_i32 s19, s32
	s_cselect_b32 s36, 1, 0
	s_cmp_gt_i32 s34, 6
	s_cselect_b32 s37, 1, 0
	s_and_b32 s36, s36, s37
	s_cselect_b32 s3, 6, s3
	s_mul_i32 s36, s3, 56
	s_add_i32 s36, s36, 32
	s_add_i32 s37, s36, 32
	s_add_i32 s38, s36, 48
	s_load_dwordx8 s[4:11], s[0:1], s36
	s_load_dwordx4 s[12:15], s[0:1], s37
	s_load_dwordx2 s[20:21], s[0:1], s38
	s_waitcnt lgkmcnt(0)
	s_mov_b32 s2, s20
	s_mul_i32 s0, s10, s11
	s_abs_i32 s1, s0
	v_cvt_f32_u32_e32 v0, s1
	s_sub_i32 s16, 0, s1
	s_sub_i32 s2, s19, s2
	s_add_i32 s2, s2, s21
	v_rcp_iflag_f32_e32 v0, v0
	s_abs_i32 s11, s2
	s_xor_b32 s3, s2, s0
	s_ashr_i32 s3, s3, 31
	v_mul_f32_e32 v0, 0x4f7ffffe, v0
	v_cvt_u32_f32_e32 v0, v0
	v_and_b32_e32 v36, 0xf0, v10
	v_mov_b32_e32 v37, 0
	v_readfirstlane_b32 s17, v0
	s_mul_i32 s16, s16, s17
	s_mul_hi_u32 s16, s17, s16
	s_add_i32 s17, s17, s16
	s_mul_hi_u32 s16, s11, s17
	s_mul_i32 s17, s16, s1
	s_sub_i32 s11, s11, s17
	s_add_i32 s18, s16, 1
	s_sub_i32 s17, s11, s1
	s_cmp_ge_u32 s11, s1
	s_cselect_b32 s16, s18, s16
	s_cselect_b32 s11, s17, s11
	s_add_i32 s17, s16, 1
	s_cmp_ge_u32 s11, s1
	s_cselect_b32 s1, s17, s16
	s_abs_i32 s11, s10
	v_cvt_f32_u32_e32 v0, s11
	s_xor_b32 s1, s1, s3
	s_sub_i32 s16, 0, s11
	s_sub_i32 s3, s1, s3
	v_rcp_iflag_f32_e32 v0, v0
	s_mul_i32 s0, s3, s0
	s_sub_i32 s0, s2, s0
	s_abs_i32 s2, s0
	v_mul_f32_e32 v0, 0x4f7ffffe, v0
	v_cvt_u32_f32_e32 v0, v0
	s_xor_b32 s1, s0, s10
	s_ashr_i32 s1, s1, 31
	v_readfirstlane_b32 s17, v0
	s_mul_i32 s16, s16, s17
	s_mul_hi_u32 s16, s17, s16
	s_add_i32 s17, s17, s16
	s_mul_hi_u32 s16, s2, s17
	s_mul_i32 s17, s16, s11
	s_sub_i32 s2, s2, s17
	s_add_i32 s18, s16, 1
	s_sub_i32 s17, s2, s11
	s_cmp_ge_u32 s2, s11
	s_cselect_b32 s16, s18, s16
	s_cselect_b32 s2, s17, s2
	s_add_i32 s17, s16, 1
	s_cmp_ge_u32 s2, s11
	s_cselect_b32 s2, s17, s16
	s_xor_b32 s2, s2, s1
	s_sub_i32 s2, s2, s1
	s_mul_i32 s1, s2, s10
	s_ashr_i32 s11, s3, 31
	s_sub_i32 s10, s0, s1
	s_mul_i32 s0, s12, s11
	s_mul_hi_u32 s1, s12, s3
	s_add_i32 s0, s1, s0
	s_mul_i32 s1, s13, s3
	s_add_i32 s1, s0, s1
	s_mul_i32 s0, s12, s3
	s_lshl_b64 s[0:1], s[0:1], 2
	s_add_u32 s4, s4, s0
	s_addc_u32 s12, s5, s1
	s_mul_i32 s0, s14, s11
	s_mul_hi_u32 s1, s14, s3
	s_add_i32 s0, s1, s0
	s_mul_i32 s1, s15, s3
	s_add_i32 s5, s0, s1
	s_lshl_b32 s0, s10, 6
	s_ashr_i32 s1, s0, 31
	s_lshl_b32 s2, s2, 7
	s_lshl_b64 s[10:11], s[0:1], 2
	s_add_u32 s10, s4, s10
	v_or_b32_e32 v28, s2, v29
	s_addc_u32 s11, s12, s11
	v_lshl_add_u64 v[32:33], s[10:11], 0, v[36:37]
	v_mad_i64_i32 v[0:1], s[10:11], v28, s9, 0
	v_lshl_add_u64 v[8:9], v[0:1], 2, v[32:33]
	v_or_b32_e32 v0, 16, v28
	v_mad_i64_i32 v[0:1], s[10:11], v0, s9, 0
	v_lshl_add_u64 v[10:11], v[0:1], 2, v[32:33]
	global_load_dwordx4 v[0:3], v[8:9], off nt
	global_load_dwordx4 v[4:7], v[10:11], off nt
	v_or_b32_e32 v8, 32, v28
	v_mad_i64_i32 v[8:9], s[10:11], v8, s9, 0
	v_lshl_add_u64 v[16:17], v[8:9], 2, v[32:33]
	v_or_b32_e32 v8, 48, v28
	v_mad_i64_i32 v[8:9], s[10:11], v8, s9, 0
	v_lshl_add_u64 v[18:19], v[8:9], 2, v[32:33]
	global_load_dwordx4 v[8:11], v[16:17], off nt
	global_load_dwordx4 v[12:15], v[18:19], off nt
	v_or_b32_e32 v16, 64, v28
	v_mad_i64_i32 v[16:17], s[10:11], v16, s9, 0
	v_lshl_add_u64 v[24:25], v[16:17], 2, v[32:33]
	v_or_b32_e32 v16, 0x50, v28
	v_mad_i64_i32 v[16:17], s[10:11], v16, s9, 0
	v_lshl_add_u64 v[26:27], v[16:17], 2, v[32:33]
	global_load_dwordx4 v[16:19], v[24:25], off nt
	global_load_dwordx4 v[20:23], v[26:27], off nt
	v_or_b32_e32 v24, 0x60, v28
	v_mad_i64_i32 v[24:25], s[10:11], v24, s9, 0
	v_lshl_add_u64 v[24:25], v[24:25], 2, v[32:33]
	v_or_b32_e32 v28, 0x70, v28
	global_load_dwordx4 v[24:27], v[24:25], off nt
	v_mad_i64_i32 v[34:35], s[10:11], v28, s9, 0
	v_lshl_add_u64 v[32:33], v[34:35], 2, v[32:33]
	global_load_dwordx4 v[32:35], v[32:33], off nt
	s_movk_i32 s1, 0x104
	v_mad_u32_u24 v28, v29, s1, v36
	v_add_u32_e32 v31, 0x1040, v28
	v_add_u32_e32 v36, 0x1048, v28
	v_add_u32_e32 v38, 0x2080, v28
	v_add_u32_e32 v39, 0x2088, v28
	v_add_u32_e32 v40, 0x30c0, v28
	v_add_u32_e32 v41, 0x30c8, v28
	v_add_u32_e32 v42, 0x4100, v28
	v_add_u32_e32 v43, 0x4108, v28
	v_add_u32_e32 v44, 0x5140, v28
	v_add_u32_e32 v45, 0x5148, v28
	s_mul_i32 s4, s14, s3
	s_lshl_b64 s[4:5], s[4:5], 1
	s_add_u32 s1, s6, s4
	s_addc_u32 s4, s7, s5
	s_ashr_i32 s3, s2, 31
	s_lshl_b64 s[2:3], s[2:3], 1
	s_add_u32 s2, s1, s2
	s_addc_u32 s3, s4, s3
	s_waitcnt vmcnt(7)
	ds_write2_b32 v28, v0, v1 offset1:1
	ds_write2_b32 v28, v2, v3 offset0:2 offset1:3
	s_waitcnt vmcnt(6)
	ds_write2_b32 v31, v4, v5 offset1:1
	ds_write2_b32 v36, v6, v7 offset1:1
	s_waitcnt vmcnt(5)
	ds_write2_b32 v38, v8, v9 offset1:1
	ds_write2_b32 v39, v10, v11 offset1:1
	s_waitcnt vmcnt(4)
	ds_write2_b32 v40, v12, v13 offset1:1
	ds_write2_b32 v41, v14, v15 offset1:1
	s_waitcnt vmcnt(3)
	ds_write2_b32 v42, v16, v17 offset1:1
	ds_write2_b32 v43, v18, v19 offset1:1
	s_waitcnt vmcnt(2)
	ds_write2_b32 v44, v20, v21 offset1:1
	ds_write2_b32 v45, v22, v23 offset1:1
	v_add_u32_e32 v0, 0x6180, v28
	s_waitcnt vmcnt(1)
	ds_write2_b32 v0, v24, v25 offset1:1
	v_add_u32_e32 v0, 0x6188, v28
	ds_write2_b32 v0, v26, v27 offset1:1
	v_add_u32_e32 v0, 0x71c0, v28
	s_waitcnt vmcnt(0)
	ds_write2_b32 v0, v32, v33 offset1:1
	v_add_u32_e32 v0, 0x71c8, v28
	ds_write2_b32 v0, v34, v35 offset1:1
	v_and_b32_e32 v0, 0x78, v30
	v_lshlrev_b32_e32 v36, 1, v0
	v_mul_u32_u24_e32 v0, 0x104, v0
	v_lshl_add_u32 v24, v29, 2, v0
	v_add_u32_e32 v25, 0x400, v24
	s_waitcnt lgkmcnt(0)
	s_barrier
	ds_read2_b32 v[4:5], v24 offset1:16
	ds_read2_b32 v[6:7], v24 offset0:130 offset1:146
	ds_read2_b32 v[8:9], v25 offset0:4 offset1:20
	ds_read2_b32 v[10:11], v25 offset0:134 offset1:150
	ds_read2_b32 v[12:13], v25 offset0:199 offset1:215
	ds_read2_b32 v[14:15], v25 offset0:69 offset1:85
	ds_read2_b32 v[16:17], v24 offset0:195 offset1:211
	ds_read2_b32 v[18:19], v24 offset0:65 offset1:81
	v_or_b32_e32 v26, s0, v29
	v_lshl_add_u64 v[20:21], s[2:3], 0, v[36:37]
	v_mad_i64_i32 v[22:23], s[0:1], v26, s8, 0
	s_waitcnt lgkmcnt(3)
	v_cvt_pk_f16_f32 v3, v10, v12
	s_waitcnt lgkmcnt(2)
	v_cvt_pk_f16_f32 v2, v8, v14
	s_waitcnt lgkmcnt(1)
	v_cvt_pk_f16_f32 v1, v6, v16
	s_waitcnt lgkmcnt(0)
	v_cvt_pk_f16_f32 v0, v4, v18
	v_lshl_add_u64 v[22:23], v[22:23], 1, v[20:21]
	global_store_dwordx4 v[22:23], v[0:3], off
	v_or_b32_e32 v4, 16, v26
	s_nop 0
	v_cvt_pk_f16_f32 v3, v11, v13
	v_cvt_pk_f16_f32 v2, v9, v15
	v_cvt_pk_f16_f32 v1, v7, v17
	v_cvt_pk_f16_f32 v0, v5, v19
	ds_read2_b32 v[6:7], v24 offset0:32 offset1:48
	ds_read2_b32 v[8:9], v24 offset0:162 offset1:178
	ds_read2_b32 v[10:11], v25 offset0:36 offset1:52
	ds_read2_b32 v[12:13], v25 offset0:166 offset1:182
	ds_read2_b32 v[14:15], v25 offset0:231 offset1:247
	ds_read2_b32 v[16:17], v25 offset0:101 offset1:117
	ds_read2_b32 v[18:19], v24 offset0:227 offset1:243
	ds_read2_b32 v[22:23], v24 offset0:97 offset1:113
	v_mad_i64_i32 v[4:5], s[0:1], v4, s8, 0
	v_lshl_add_u64 v[4:5], v[4:5], 1, v[20:21]
	global_store_dwordx4 v[4:5], v[0:3], off
	v_or_b32_e32 v4, 32, v26
	v_mad_i64_i32 v[4:5], s[0:1], v4, s8, 0
	s_waitcnt lgkmcnt(3)
	v_cvt_pk_f16_f32 v3, v12, v14
	s_waitcnt lgkmcnt(2)
	v_cvt_pk_f16_f32 v2, v10, v16
	s_waitcnt lgkmcnt(1)
	v_cvt_pk_f16_f32 v1, v8, v18
	s_waitcnt lgkmcnt(0)
	v_cvt_pk_f16_f32 v0, v6, v22
	v_lshl_add_u64 v[4:5], v[4:5], 1, v[20:21]
	global_store_dwordx4 v[4:5], v[0:3], off
	v_or_b32_e32 v4, 48, v26
	v_mad_i64_i32 v[4:5], s[0:1], v4, s8, 0
	v_cvt_pk_f16_f32 v3, v13, v15
	v_cvt_pk_f16_f32 v2, v11, v17
	v_cvt_pk_f16_f32 v1, v9, v19
	v_cvt_pk_f16_f32 v0, v7, v23
	v_lshl_add_u64 v[4:5], v[4:5], 1, v[20:21]
	global_store_dwordx4 v[4:5], v[0:3], off
	s_endpgm
.LBB3_14:
	s_endpgm
	s_endpgm
	s_endpgm
	s_endpgm
	s_endpgm
	s_endpgm
	s_endpgm
	s_endpgm
	s_endpgm
	s_endpgm
	s_endpgm
	s_endpgm
	s_endpgm
	s_endpgm
	s_endpgm
	s_endpgm
	s_endpgm
	s_endpgm
	s_endpgm
